# out-projection to norm3 barrier also XCD-local: norm3 row groups remapped onto the XCD that wrote their row tile
# baseline (speedup 1.0000x reference)
.LBB0_1251:
	s_andn2_b64 vcc, exec, s[0:1]
	s_cbranch_vccnz .LBB0_1545
	v_readlane_b32 s0, v245, 60
	v_readlane_b32 s1, v245, 61
	s_waitcnt vmcnt(15)
	v_mov_b32_e32 v102, v0
	s_andn2_b64 vcc, exec, s[0:1]
	s_cbranch_vccnz .LBB0_1493
	v_readlane_b32 s8, v244, 47
	v_readlane_b32 s10, v244, 49
	v_readlane_b32 s11, v244, 50
	s_nop 4
	global_load_dwordx4 v[2:5], v195, s[10:11]
	global_load_dwordx4 v[6:9], v195, s[10:11] offset:16
	global_load_dwordx4 v[10:13], v195, s[10:11] offset:32
	global_load_dwordx4 v[14:17], v195, s[10:11] offset:48
	v_readlane_b32 s6, v244, 22
	s_lshl_b32 s0, s6, 13
	v_readlane_b32 s4, v242, 20
	s_waitcnt vmcnt(9)
	v_lshlrev_b32_e32 v26, 2, v102
	v_readlane_b32 s5, v242, 21
	s_add_u32 s0, s4, s0
	s_waitcnt vmcnt(8)
	v_and_b32_e32 v24, 64, v196
	v_add_u32_e32 v1, 0, v26
	s_addc_u32 s1, s5, 0
	v_add_u32_e32 v22, 64, v24
	v_add_u32_e32 v132, 0x11800, v1
	v_xor_b32_e32 v1, 16, v196
	s_add_u32 s34, s0, 0x1000
	v_cmp_lt_i32_e32 vcc, v1, v22
	v_and_b32_e32 v129, 63, v102
	s_addc_u32 s35, s1, 0
	s_lshl_b32 s0, s6, 3
	v_cndmask_b32_e32 v1, v196, v1, vcc
	v_readlane_b32 s9, v244, 48
	v_readlane_b32 s12, v244, 51
	v_readlane_b32 s13, v244, 52
	v_readlane_b32 s14, v244, 53
	v_readlane_b32 s15, v244, 54
	v_writelane_b32 v244, s0, 58
	v_cmp_eq_u32_e64 s[0:1], 0, v129
	v_lshlrev_b32_e32 v133, 2, v1
	v_xor_b32_e32 v1, 32, v196
	v_writelane_b32 v244, s0, 59
	v_cmp_lt_i32_e32 vcc, v1, v22
	s_waitcnt vmcnt(10)
	v_and_b32_e32 v128, 15, v102
	v_writelane_b32 v244, s1, 60
	v_cmp_gt_i32_e64 s[0:1], 16, v102
	v_cndmask_b32_e32 v1, v196, v1, vcc
	v_lshlrev_b32_e32 v134, 2, v1
	v_writelane_b32 v244, s0, 61
	v_lshlrev_b32_e32 v1, 2, v128
	v_ashrrev_i32_e32 v109, 6, v102
	v_writelane_b32 v244, s1, 62
	s_waitcnt vmcnt(4)
	v_add_u32_e32 v18, 0, v1
	s_movk_i32 s0, 0x440
	v_add_u32_e32 v135, 0x11800, v18
	v_mul_lo_u32 v18, v109, s0
	v_readlane_b32 s0, v242, 37
	v_lshlrev_b32_e32 v104, 3, v129
	v_mov_b32_e32 v105, v195
	v_add_u32_e32 v27, s0, v18
	v_cmp_gt_u32_e64 s[0:1], 16, v129
	v_lshlrev_b32_e32 v20, 2, v129
	v_and_b32_e32 v21, 0xffffffc0, v102
	v_writelane_b32 v244, s0, 63
	v_lshlrev_b64 v[18:19], v102, -1
	v_not_b32_e32 v108, v18
	v_writelane_b32 v241, s1, 0
	v_readlane_b32 s0, v246, 27
	v_readlane_b32 s1, v246, 28
	v_add_u32_e32 v29, v27, v1
	v_not_b32_e32 v1, v19
	v_lshl_add_u64 v[106:107], s[0:1], 0, v[104:105]
	v_readlane_b32 s0, v242, 36
	v_xor_b32_e32 v31, 1, v196
	v_cmp_lt_i32_e32 vcc, v31, v22
	v_add3_u32 v105, s0, v20, v21
	v_add_u32_e32 v136, s0, v26
	s_lshl_b32 s0, s6, 10
	v_lshl_add_u32 v18, v102, 6, s0
	v_readlane_b32 s0, v243, 38
	v_ashrrev_i32_e32 v19, 31, v18
	v_readlane_b32 s1, v243, 39
	v_cndmask_b32_e32 v31, v196, v31, vcc
	v_lshlrev_b32_e32 v138, 2, v31
	v_lshl_add_u64 v[110:111], v[18:19], 2, s[0:1]
	v_readlane_b32 s0, v242, 38
	v_xor_b32_e32 v31, 2, v196
	v_cmp_lt_i32_e32 vcc, v31, v22
	v_add_u32_e32 v137, s0, v26
	s_add_i32 s0, 0, 0x11000
	v_add_u32_e32 v145, s0, v26
	v_readlane_b32 s0, v242, 39
	v_cndmask_b32_e32 v31, v196, v31, vcc
	v_lshlrev_b32_e32 v139, 2, v31
	v_add_u32_e32 v146, s0, v26
	v_readlane_b32 s0, v242, 40
	v_xor_b32_e32 v31, 4, v196
	v_cmp_lt_i32_e32 vcc, v31, v22
	v_add_u32_e32 v147, s0, v26
	v_readlane_b32 s0, v242, 41
	v_cndmask_b32_e32 v31, v196, v31, vcc
	v_lshlrev_b32_e32 v140, 2, v31
	v_add_u32_e32 v148, s0, v26
	v_readlane_b32 s0, v242, 42
	v_xor_b32_e32 v31, 8, v196
	v_cmp_lt_i32_e32 vcc, v31, v22
	v_add_u32_e32 v149, s0, v26
	v_readlane_b32 s0, v242, 43
	v_lshlrev_b32_e32 v18, 4, v102
	v_cndmask_b32_e32 v22, v196, v31, vcc
	v_add_u32_e32 v150, s0, v26
	v_readlane_b32 s0, v242, 44
	v_lshlrev_b32_e32 v141, 2, v22
	v_and_b32_e32 v22, 0x3f0, v18
	v_add_u32_e32 v151, s0, v26
	v_readlane_b32 s0, v242, 45
	v_add_u32_e32 v153, 0, v22
	v_lshlrev_b32_e32 v194, 5, v129
	v_add_u32_e32 v152, s0, v26
	v_cmp_eq_u32_e64 s[0:1], 15, v129
	v_or_b32_e32 v22, 0x200, v104
	v_bfe_u32 v23, v102, 4, 2
	v_writelane_b32 v241, s0, 1
	v_lshl_add_u64 v[112:113], s[34:35], 0, v[194:195]
	v_lshlrev_b32_e32 v194, 2, v22
	v_writelane_b32 v241, s1, 2
	v_cmp_eq_u32_e64 s[0:1], 14, v129
	v_add_u32_e32 v25, 0, v21
	v_lshlrev_b32_e32 v28, 2, v23
	v_writelane_b32 v241, s0, 3
	v_lshl_add_u64 v[114:115], s[34:35], 0, v[194:195]
	v_and_b32_e32 v194, 48, v102
	v_writelane_b32 v241, s1, 4
	v_cmp_eq_u32_e64 s[0:1], 13, v129
	v_add_u32_e32 v131, 0x11000, v25
	v_add_u32_e32 v142, 0x11010, v25
	v_writelane_b32 v241, s0, 5
	v_add_u32_e32 v143, 0x11020, v25
	v_add_u32_e32 v144, 0x11030, v25
	v_writelane_b32 v241, s1, 6
	v_cmp_eq_u32_e64 s[0:1], 12, v129
	v_or_b32_e32 v25, v24, v28
	v_add_u32_e32 v20, 0x2000, v18
	v_writelane_b32 v241, s0, 7
	v_lshlrev_b32_e32 v154, 2, v25
	v_or_b32_e32 v25, 1, v28
	v_writelane_b32 v241, s1, 8
	v_cmp_eq_u32_e64 s[0:1], 11, v129
	v_and_b32_e32 v175, 0x7ffffffe, v109
	v_mul_u32_u24_e32 v30, 0x44, v128
	v_writelane_b32 v241, s0, 9
	v_ashrrev_i32_e32 v19, 31, v18
	v_ashrrev_i32_e32 v21, 31, v20
	v_writelane_b32 v241, s1, 10
	v_cmp_eq_u32_e64 s[0:1], 10, v129
	v_mul_u32_u24_e32 v23, 0x110, v23
	v_or_b32_e32 v26, v24, v25
	v_writelane_b32 v241, s0, 11
	v_mul_u32_u24_e32 v25, 0x44, v25
	v_lshlrev_b32_e32 v158, 2, v24
	v_writelane_b32 v241, s1, 12
	v_cmp_eq_u32_e64 s[0:1], 9, v129
	v_lshlrev_b32_e32 v130, 4, v109
	v_cmp_lt_i32_e64 s[58:59], 0, v109
	v_writelane_b32 v241, s0, 13
	v_ashrrev_i32_e32 v103, 31, v102
	v_lshlrev_b32_e32 v155, 2, v26
	v_writelane_b32 v241, s1, 14
	v_cmp_eq_u32_e64 s[0:1], 8, v129
	v_or_b32_e32 v156, 8, v154
	v_or_b32_e32 v157, 12, v154
	v_writelane_b32 v241, s0, 15
	v_or_b32_e32 v159, 4, v158
	v_or_b32_e32 v160, 8, v158
	v_writelane_b32 v241, s1, 16
	v_cmp_eq_u32_e64 s[0:1], 7, v129
	v_or_b32_e32 v161, 12, v158
	v_or_b32_e32 v162, 16, v158
	v_writelane_b32 v241, s0, 17
	v_or_b32_e32 v163, 20, v158
	v_or_b32_e32 v164, 24, v158
	v_writelane_b32 v241, s1, 18
	v_cmp_eq_u32_e64 s[0:1], 6, v129
	v_or_b32_e32 v165, 28, v158
	v_or_b32_e32 v166, 32, v158
	v_writelane_b32 v241, s0, 19
	v_or_b32_e32 v167, 36, v158
	v_or_b32_e32 v168, 40, v158
	v_writelane_b32 v241, s1, 20
	v_cmp_eq_u32_e64 s[0:1], 5, v129
	v_or_b32_e32 v169, 44, v158
	v_or_b32_e32 v170, 48, v158
	v_writelane_b32 v241, s0, 21
	v_or_b32_e32 v171, 52, v158
	v_or_b32_e32 v172, 56, v158
	v_writelane_b32 v241, s1, 22
	v_cmp_eq_u32_e64 s[0:1], 4, v129
	v_or_b32_e32 v173, 60, v158
	v_lshl_add_u64 v[118:119], v[18:19], 2, s[8:9]
	v_writelane_b32 v241, s0, 23
	v_lshl_add_u64 v[120:121], v[20:21], 2, s[8:9]
	v_or_b32_e32 v174, 0x70, v128
	v_writelane_b32 v241, s1, 24
	v_cmp_eq_u32_e64 s[0:1], 3, v129
	v_add_u32_e32 v176, 0, v18
	v_lshlrev_b32_e32 v177, 2, v22
	v_writelane_b32 v241, s0, 25
	v_add_u32_e32 v178, v29, v23
	v_add_u32_e32 v179, v29, v25
	v_writelane_b32 v241, s1, 26
	v_cmp_eq_u32_e64 s[0:1], 2, v129
	v_add_u32_e32 v180, v27, v30
	v_readlane_b32 s47, v242, 32
	v_writelane_b32 v241, s0, 27
	s_nop 1
	v_writelane_b32 v241, s1, 28
	v_cmp_eq_u32_e64 s[0:1], 1, v129
	s_nop 1
	v_writelane_b32 v241, s0, 29
	s_nop 1
	v_writelane_b32 v241, s1, 30
	v_readlane_b32 s0, v246, 23
	v_readlane_b32 s1, v246, 24
	s_nop 1
	v_lshl_add_u64 v[116:117], s[0:1], 0, v[194:195]
	v_cmp_ne_u32_e64 s[0:1], 1, v109
	s_nop 1
	v_writelane_b32 v241, s0, 31
	s_nop 1
	v_writelane_b32 v241, s1, 32
	v_cmp_ne_u32_e64 s[0:1], v109, v175
	s_nop 1
	v_writelane_b32 v241, s0, 33
	s_nop 1
	v_writelane_b32 v241, s1, 34
	s_lshr_b32 s0, s47, 4
	s_lshl_b32 s0, s0, 3
	s_and_b32 s1, s47, 7
	s_add_i32 s0, s0, s1
	s_lshl_b32 s0, s0, 1
	s_bfe_u32 s1, s47, 0x10003
	s_add_i32 s47, s0, s1
	s_branch .LBB0_1255
